# down GEMM: remap lanes of the f32 weight loads so each wave reads 128 contiguous bytes per k-row (full cache lines); LDS image unchanged
# speedup vs baseline: 1.0647x; 1.0647x over previous
; #define PG8_BWAIT(n) asm volatile("s_waitcnt vmcnt(" #n ")" : "+v"(bv[0]), "+v"(bv[1]), "+v"(bv[2]), "+v"(bv[3]), "+v"(bv[4]), "+v"(bv[5]), "+v"(bv[6]), "+v"(bv[7]) :: "memory")
; #define PG8_STAGE_A(bufoff, V0, V1, kb) do { \
;         __builtin_amdgcn_global_load_lds((const unsigned*)((Abase + (kb)) + (V0)), (LAS unsigned*)(lds + (bufoff) + ldsw), 16, 0, 0); \
;         __builtin_amdgcn_global_load_lds((const unsigned*)((Abase + (kb)) + (V1)), (LAS unsigned*)(lds + (bufoff) + ldsw + 8192), 16, 0, 0); } while (0)
; #define PG8_SCHED __builtin_amdgcn_sched_barrier(0)
;     __device__ __forceinline__ int blane(int rho) const { if constexpr (NPN == 2) return rho; else return 64 * (rho >> 5) + 16 * ((rho >> 3) & 3) + (rho & 7); }
; template <class Epi, class Sched, bool ALIGN_EPI>
; __device__ __forceinline__ void gemm_phase(LAS unsigned char* lds, const Gemm g, const Sched& S, const Epi& E) {
;     ...
;     [[maybe_unused]] const int bh = wid >> 2, brg = ((wid & 3) << 3) + (lane & 7), bkg = lane >> 3;
;     [[maybe_unused]] const int brho = 32 * (brg >> 3) + 8 * (brg & 3) + 4 * ((brg >> 2) & 1);
;     [[maybe_unused]] const int bwofs = bh * HTB + lds_byte(4 * brg, 8 * bkg);
;     [[maybe_unused]] const unsigned blane = (unsigned)(S.blane(brho) + 8 * bkg * Sched::LDN) * 4u;
;     [[maybe_unused]] const unsigned bwaddr = ((unsigned)(size_t)lds + (unsigned)bwofs) | ((unsigned)(brg & 3) << 6);
;     ...
;         PG8_BISSUE(pbc);
;         PG8_STAGE_A(PG8_SA(0, 0), vc00, vc01, 0u); PG8_STAGE_A(PG8_SA(0, 1), vc10, vc11, 0u); PG8_STAGE_A(PG8_SA(1, 0), vc00, vc01, 128u);
;         PG8_BWAIT(0); PG8_BCOMMIT(0); PG8_SCHED; PG8_BISSUE(pbc + (size_t)64 * Sched::LDN);
.LBB0_2429:
	s_ashr_i32 s6, s7, 6
	s_and_b32 s0, s6, 3
	v_and_b32_e32 v36, 3, v1
	s_lshl_b32 s12, s6, 10
	v_and_b32_e32 v2, 56, v1
	v_and_b32_e32 v3, 4, v1
	v_lshlrev_b32_e32 v4, 4, v36
	s_lshl_b32 s6, s0, 6
	v_or3_b32 v3, v4, v3, s6
	v_lshlrev_b32_e32 v2, 12, v2
	v_lshl_or_b32 v240, v3, 2, v2
	v_and_b32_e32 v3, 7, v1
	v_lshl_add_u32 v3, v3, 4, v2
	v_lshrrev_b32_e32 v4, 8, v1
	v_mul_u32_u24_e32 v4, 0x60, v4
	v_lshrrev_b32_e32 v240, 6, v1
	v_and_b32_e32 v240, 3, v240
	v_lshl_add_u32 v4, v240, 8, v4
	v_add_u32_e32 v240, v3, v4
	v_mov_b32_e32 v2, v1
	v_mov_b32_e32 v241, 1
	v_ashrrev_i32_e32 v4, 31, v2
	v_lshrrev_b32_e32 v4, 26, v4
	v_lshlrev_b32_e32 v3, 4, v2
	v_add_u32_e32 v4, v2, v4
	v_bfe_i32 v2, v2, 27, 1
	v_lshrrev_b32_e32 v2, 22, v2
	v_add_u32_e32 v2, v3, v2
	v_and_b32_e32 v2, 0xfffffc00, v2
	v_sub_u32_e32 v2, v3, v2
	v_lshrrev_b32_e32 v5, 4, v2
	v_bitop3_b32 v2, v5, v2, 32 bitop3:0x6c
	v_ashrrev_i32_e32 v6, 31, v2
	v_lshrrev_b32_e32 v6, 26, v6
	v_add_u32_e32 v6, v2, v6
	v_ashrrev_i32_e32 v7, 6, v6
	v_and_b32_e32 v6, 0xc0, v6
	v_ashrrev_i32_e32 v4, 6, v4
	v_sub_u32_e32 v2, v2, v6
	v_lshlrev_b32_e32 v5, 3, v4
	v_lshlrev_b32_e32 v4, 5, v4
	v_ashrrev_i16_sdwa v2, v241, sext(v2) dst_sel:DWORD dst_unused:UNUSED_PAD src0_sel:DWORD src1_sel:BYTE_0
	v_and_b32_e32 v4, 32, v4
	v_bfe_i32 v2, v2, 0, 16
	v_add_lshl_u32 v34, v4, v2, 1
	v_add_u32_e32 v2, 0x2000, v3
	v_ashrrev_i32_e32 v3, 31, v2
	v_lshrrev_b32_e32 v3, 22, v3
	v_add_u32_e32 v3, v2, v3
	v_ashrrev_i32_e32 v3, 10, v3
	v_mul_i32_i24_e32 v4, 0x400, v3
	v_sub_u32_e32 v2, v2, v4
	v_lshrrev_b32_e32 v4, 4, v2
	v_bitop3_b32 v2, v4, v2, 32 bitop3:0x6c
	v_ashrrev_i32_e32 v6, 31, v2
	v_lshrrev_b32_e32 v6, 26, v6
	v_and_b32_e32 v5, -16, v5
	v_add_u32_e32 v6, v2, v6
	v_add_u32_e32 v5, v7, v5
	v_ashrrev_i32_e32 v7, 6, v6
	v_and_b32_e32 v6, 0xc0, v6
	v_sub_u32_e32 v2, v2, v6
	s_ashr_i32 s1, s7, 8
	v_lshlrev_b32_e32 v4, 3, v3
	v_lshlrev_b32_e32 v3, 5, v3
	v_ashrrev_i16_sdwa v2, v241, sext(v2) dst_sel:DWORD dst_unused:UNUSED_PAD src0_sel:DWORD src1_sel:BYTE_0
	s_lshl_b32 s8, s1, 14
	v_and_b32_e32 v4, -16, v4
	v_and_b32_e32 v3, 32, v3
	v_bfe_i32 v2, v2, 0, 16
	s_add_i32 s13, s8, 0
	v_add_u32_e32 v4, v7, v4
	v_add_lshl_u32 v35, v3, v2, 1
	v_add_u32_e32 v2, s41, v5
	s_add_i32 s8, s34, -1
	v_min_i32_e32 v37, s8, v2
	v_add_u32_e32 v2, s41, v4
	s_add_i32 s9, s41, 0x80
	v_min_i32_e32 v38, s8, v2
	v_add_u32_e32 v2, s9, v5
	v_min_i32_e32 v39, s8, v2
	v_add_u32_e32 v2, s9, v4
	v_min_i32_e32 v40, s8, v2
	s_add_u32 s8, s76, s4
	s_addc_u32 s9, s77, s5
	s_lshl_b32 s4, s33, 8
	s_ashr_i32 s5, s4, 31
	s_lshl_b64 s[4:5], s[4:5], 2
	s_add_u32 s10, s8, s4
	s_addc_u32 s11, s9, s5
	s_lshl_b32 s4, s1, 3
	s_ashr_i32 s5, s4, 31
	s_lshl_b64 s[8:9], s[4:5], 2
	s_add_u32 s4, s10, s8
	s_addc_u32 s5, s11, s9
	s_add_u32 s10, s4, 0x1000
	global_load_dwordx4 v[2:5], v240, s[4:5] offset:0
	s_addc_u32 s11, s5, 0
	global_load_dwordx4 v[6:9], v240, s[10:11] offset:0
	s_add_u32 s10, s4, 0x2000
	s_addc_u32 s11, s5, 0
	global_load_dwordx4 v[10:13], v240, s[10:11] offset:0
	s_add_u32 s10, s4, 0x3000
	s_addc_u32 s11, s5, 0
	global_load_dwordx4 v[14:17], v240, s[10:11] offset:0
	s_add_u32 s10, s4, 0x4000
	s_addc_u32 s11, s5, 0
	global_load_dwordx4 v[18:21], v240, s[10:11] offset:0
	s_add_u32 s10, s4, 0x5000
	s_addc_u32 s11, s5, 0
	global_load_dwordx4 v[22:25], v240, s[10:11] offset:0
	s_add_u32 s10, s4, 0x6000
	s_addc_u32 s11, s5, 0
	global_load_dwordx4 v[26:29], v240, s[10:11] offset:0
	s_add_u32 s10, s4, 0x7000
	s_addc_u32 s11, s5, 0
	global_load_dwordx4 v[30:33], v240, s[10:11] offset:0
	s_add_i32 s35, s12, 0
	v_readlane_b32 s10, v254, 53
	v_lshl_add_u32 v226, v37, 9, v34
	s_mov_b32 m0, s35
	v_readlane_b32 s11, v254, 54
	s_add_i32 s36, s35, 0x2000
	v_lshl_add_u32 v228, v38, 9, v35
	s_add_i32 s37, s35, 0x4000
	v_lshl_add_u32 v230, v39, 9, v34
	s_add_i32 s38, s35, 0x6000
	global_load_lds_dwordx4 v226, s[10:11]
	s_mov_b32 m0, s36
	v_lshl_add_u32 v232, v40, 9, v35
	global_load_lds_dwordx4 v228, s[10:11]
	s_mov_b32 m0, s37
	v_lshlrev_b32_e32 v34, 2, v1
	global_load_lds_dwordx4 v230, s[10:11]
	s_mov_b32 m0, s38
	v_and_b32_e32 v35, 16, v34
	global_load_lds_dwordx4 v232, s[10:11]
	s_add_u32 s10, s90, 0x27340080
	s_addc_u32 s11, s91, 0
	s_add_i32 s39, s35, 0x8000
	s_mov_b32 m0, s39
	s_add_i32 s40, s35, 0xa000
	global_load_lds_dwordx4 v226, s[10:11]
	s_mov_b32 m0, s40
	v_lshl_or_b32 v35, s0, 5, v35
	global_load_lds_dwordx4 v228, s[10:11]
	v_lshrrev_b32_e32 v35, 3, v35
	v_bfe_u32 v37, v1, 5, 1
	v_or_b32_e32 v35, v35, v37
	v_lshlrev_b32_e32 v37, 8, v1
	v_lshlrev_b32_e32 v38, 1, v1
	v_lshlrev_b32_e32 v39, 10, v35
	v_lshlrev_b32_e32 v35, 4, v1
	v_and_b32_e32 v37, 0x300, v37
	v_and_b32_e32 v38, 48, v38
	v_and_b32_e32 v40, 32, v35
	v_bitop3_b32 v37, v37, v40, v38 bitop3:0x36
	v_add3_u32 v37, s13, v37, v39
	v_lshl_or_b32 v242, v36, 6, v37
	v_lshrrev_b32_e32 v39, 8, v1
	v_lshrrev_b32_e32 v36, 2, v1
	v_and_b32_e32 v36, 1, v36
	v_lshl_or_b32 v36, v39, 1, v36
	v_lshlrev_b32_e32 v37, 8, v36
	v_lshl_or_b32 v37, v36, 6, v37
	v_lshlrev_b32_e32 v38, 1, v1
	v_and_b32_e32 v38, 48, v38
	v_or_b32_e32 v37, v37, v38
	v_lshlrev_b32_e32 v38, 5, v39
	v_xor_b32_e32 v37, v37, v38
	v_lshlrev_b32_e32 v38, 13, v1
	v_and_b32_e32 v38, 0x4000, v38
	v_or_b32_e32 v37, v37, v38
	v_and_b32_e32 v38, 1, v1
	v_bfe_u32 v36, v1, 5, 1
	v_lshl_or_b32 v38, v38, 1, v36
	v_lshrrev_b32_e32 v39, 6, v1
	v_and_b32_e32 v39, 3, v39
	v_lshl_or_b32 v38, v39, 2, v38
	v_lshl_or_b32 v242, v38, 10, v37
	v_mov_b32_e32 v36, v242
	s_waitcnt vmcnt(0)
; #define PG8_BWAIT(n) asm volatile("s_waitcnt vmcnt(" #n ")" : "+v"(bv[0]), "+v"(bv[1]), "+v"(bv[2]), "+v"(bv[3]), "+v"(bv[4]), "+v"(bv[5]), "+v"(bv[6]), "+v"(bv[7]) :: "memory")
; #define PG8_WAIT_V(n) asm volatile("s_waitcnt vmcnt(" #n ")" ::: "memory")
; #define PG8_WAIT_L(n) asm volatile("s_waitcnt lgkmcnt(" #n ")" ::: "memory")
; #define PG8_BAR __builtin_amdgcn_s_barrier()
; #define PG8_SCHED __builtin_amdgcn_sched_barrier(0)
; template <class Epi, class Sched, bool ALIGN_EPI>
; __device__ __forceinline__ void gemm_phase(LAS unsigned char* lds, const Gemm g, const Sched& S, const Epi& E) {
;     ...
;         PG8_BWAIT(0); PG8_BCOMMIT(0); PG8_SCHED; PG8_BISSUE(pbc + (size_t)64 * Sched::LDN);
;         PG8_BWAIT(0); PG8_BCOMMIT(1); PG8_SCHED; PG8_BISSUE(pbc + (size_t)128 * Sched::LDN);
;         PG8_WAIT_V(8); PG8_WAIT_L(0);
;         if (wr == 1) PG8_BAR;
;         PG8_BAR; PG8_BAR;
	s_mov_b32 s11, 0
	v_add_u32_e32 v40, 0x10000, v36
	v_cvt_pk_bf16_f32 v36, v2, v6
	v_cvt_pk_bf16_f32 v37, v10, v14
	v_cvt_pk_bf16_f32 v38, v18, v22
	v_cvt_pk_bf16_f32 v39, v26, v30
	ds_write_b128 v40, v[36:39]
	s_nop 1
	v_cvt_pk_bf16_f32 v36, v3, v7
	v_cvt_pk_bf16_f32 v37, v11, v15
	v_cvt_pk_bf16_f32 v38, v19, v23
	v_cvt_pk_bf16_f32 v39, v27, v31
	v_xor_b32_e32 v2, 64, v40
	ds_write_b128 v2, v[36:39]
	s_nop 1
	v_cvt_pk_bf16_f32 v36, v4, v8
	v_cvt_pk_bf16_f32 v37, v12, v16
	v_cvt_pk_bf16_f32 v38, v20, v24
	v_cvt_pk_bf16_f32 v39, v28, v32
	v_xor_b32_e32 v2, 0x80, v40
	ds_write_b128 v2, v[36:39]
	s_nop 1
	v_cvt_pk_bf16_f32 v2, v5, v9
	v_cvt_pk_bf16_f32 v3, v13, v17
	v_cvt_pk_bf16_f32 v4, v21, v25
	v_cvt_pk_bf16_f32 v5, v29, v33
	v_xor_b32_e32 v6, 0xc0, v40
	ds_write_b128 v6, v[2:5]
	s_nop 1
	s_add_u32 s12, s4, 0x40000
	s_addc_u32 s13, s5, 0
	s_add_u32 s14, s12, 0x1000
	global_load_dwordx4 v[2:5], v240, s[12:13] offset:0
	s_addc_u32 s15, s13, 0
	global_load_dwordx4 v[6:9], v240, s[14:15] offset:0
	s_add_u32 s14, s12, 0x2000
	s_addc_u32 s15, s13, 0
	global_load_dwordx4 v[10:13], v240, s[14:15] offset:0
	s_add_u32 s14, s12, 0x3000
	s_addc_u32 s15, s13, 0
	global_load_dwordx4 v[14:17], v240, s[14:15] offset:0
	s_add_u32 s14, s12, 0x4000
	s_addc_u32 s15, s13, 0
	global_load_dwordx4 v[18:21], v240, s[14:15] offset:0
	s_add_u32 s14, s12, 0x5000
	s_addc_u32 s15, s13, 0
	global_load_dwordx4 v[22:25], v240, s[14:15] offset:0
	s_add_u32 s14, s12, 0x6000
	s_addc_u32 s15, s13, 0
	global_load_dwordx4 v[26:29], v240, s[14:15] offset:0
	s_add_u32 s12, s12, 0x7000
	s_addc_u32 s13, s13, 0
	global_load_dwordx4 v[30:33], v240, s[12:13] offset:0
	v_mov_b32_e32 v36, v242
	s_waitcnt vmcnt(0)
	s_nop 0
	v_add_u32_e32 v40, 0x18000, v36
	v_cvt_pk_bf16_f32 v36, v2, v6
	v_cvt_pk_bf16_f32 v37, v10, v14
	v_cvt_pk_bf16_f32 v38, v18, v22
	v_cvt_pk_bf16_f32 v39, v26, v30
	ds_write_b128 v40, v[36:39]
	s_nop 1
	v_cvt_pk_bf16_f32 v36, v3, v7
	v_cvt_pk_bf16_f32 v37, v11, v15
	v_cvt_pk_bf16_f32 v38, v19, v23
	v_cvt_pk_bf16_f32 v39, v27, v31
	v_xor_b32_e32 v2, 64, v40
	ds_write_b128 v2, v[36:39]
	s_nop 1
	v_cvt_pk_bf16_f32 v36, v4, v8
	v_cvt_pk_bf16_f32 v37, v12, v16
	v_cvt_pk_bf16_f32 v38, v20, v24
	v_cvt_pk_bf16_f32 v39, v28, v32
	v_xor_b32_e32 v2, 0x80, v40
	ds_write_b128 v2, v[36:39]
	s_nop 1
	v_cvt_pk_bf16_f32 v2, v5, v9
	v_cvt_pk_bf16_f32 v3, v13, v17
	v_cvt_pk_bf16_f32 v4, v21, v25
	v_cvt_pk_bf16_f32 v5, v29, v33
	v_xor_b32_e32 v6, 0xc0, v40
	ds_write_b128 v6, v[2:5]
	s_nop 1
	s_add_u32 s12, s4, 0x80000
	s_addc_u32 s13, s5, 0
	s_add_u32 s14, s12, 0x1000
	global_load_dwordx4 v[2:5], v240, s[12:13] offset:0
	s_addc_u32 s15, s13, 0
	global_load_dwordx4 v[6:9], v240, s[14:15] offset:0
	s_add_u32 s14, s12, 0x2000
	s_addc_u32 s15, s13, 0
	global_load_dwordx4 v[10:13], v240, s[14:15] offset:0
	s_add_u32 s14, s12, 0x3000
	s_addc_u32 s15, s13, 0
	global_load_dwordx4 v[14:17], v240, s[14:15] offset:0
	s_add_u32 s14, s12, 0x4000
	s_addc_u32 s15, s13, 0
	global_load_dwordx4 v[18:21], v240, s[14:15] offset:0
	s_add_u32 s14, s12, 0x5000
	s_addc_u32 s15, s13, 0
	global_load_dwordx4 v[22:25], v240, s[14:15] offset:0
	s_add_u32 s14, s12, 0x6000
	s_addc_u32 s15, s13, 0
	global_load_dwordx4 v[26:29], v240, s[14:15] offset:0
	s_add_u32 s12, s12, 0x7000
	s_addc_u32 s13, s13, 0
	global_load_dwordx4 v[30:33], v240, s[12:13] offset:0
	s_waitcnt vmcnt(8)
	s_waitcnt lgkmcnt(0)
	s_cmp_eq_u32 s1, 1
	s_cselect_b64 s[12:13], -1, 0
	s_cmp_lg_u32 s1, 1
	s_cbranch_scc1 .LBB0_2431
	s_barrier

; #define PG8_BWAIT(n) asm volatile("s_waitcnt vmcnt(" #n ")" : "+v"(bv[0]), "+v"(bv[1]), "+v"(bv[2]), "+v"(bv[3]), "+v"(bv[4]), "+v"(bv[5]), "+v"(bv[6]), "+v"(bv[7]) :: "memory")
; #define PG8_STAGE_A(bufoff, V0, V1, kb) do { \
;         __builtin_amdgcn_global_load_lds((const unsigned*)((Abase + (kb)) + (V0)), (LAS unsigned*)(lds + (bufoff) + ldsw), 16, 0, 0); \
;         __builtin_amdgcn_global_load_lds((const unsigned*)((Abase + (kb)) + (V1)), (LAS unsigned*)(lds + (bufoff) + ldsw + 8192), 16, 0, 0); } while (0)
; #define PG8_SCHED __builtin_amdgcn_sched_barrier(0)
;     __device__ __forceinline__ int blane(int rho) const { if constexpr (NPN == 2) return rho; else return 64 * (rho >> 5) + 16 * ((rho >> 3) & 3) + (rho & 7); }
; template <class Epi, class Sched, bool ALIGN_EPI>
; __device__ __forceinline__ void gemm_phase(LAS unsigned char* lds, const Gemm g, const Sched& S, const Epi& E) {
;     ...
;     [[maybe_unused]] const int bh = wid >> 2, brg = ((wid & 3) << 3) + (lane & 7), bkg = lane >> 3;
;     [[maybe_unused]] const int brho = 32 * (brg >> 3) + 8 * (brg & 3) + 4 * ((brg >> 2) & 1);
;     [[maybe_unused]] const int bwofs = bh * HTB + lds_byte(4 * brg, 8 * bkg);
;     [[maybe_unused]] const unsigned blane = (unsigned)(S.blane(brho) + 8 * bkg * Sched::LDN) * 4u;
;     [[maybe_unused]] const unsigned bwaddr = ((unsigned)(size_t)lds + (unsigned)bwofs) | ((unsigned)(brg & 3) << 6);
;     ...
;         PG8_BISSUE(pbc);
;         PG8_STAGE_A(PG8_SA(0, 0), vc00, vc01, 0u); PG8_STAGE_A(PG8_SA(0, 1), vc10, vc11, 0u); PG8_STAGE_A(PG8_SA(1, 0), vc00, vc01, 128u);
;         PG8_BWAIT(0); PG8_BCOMMIT(0); PG8_SCHED; PG8_BISSUE(pbc + (size_t)64 * Sched::LDN);
.LBB0_4889:
	s_ashr_i32 s4, s5, 6
	s_and_b32 s0, s4, 3
	v_and_b32_e32 v36, 3, v1
	s_lshl_b32 s10, s4, 10
	v_and_b32_e32 v2, 56, v1
	v_and_b32_e32 v3, 4, v1
	v_lshlrev_b32_e32 v4, 4, v36
	s_lshl_b32 s4, s0, 6
	v_or3_b32 v3, v4, v3, s4
	v_lshlrev_b32_e32 v2, 12, v2
	v_lshl_or_b32 v240, v3, 2, v2
	v_and_b32_e32 v3, 7, v1
	v_lshl_add_u32 v3, v3, 4, v2
	v_lshrrev_b32_e32 v4, 8, v1
	v_mul_u32_u24_e32 v4, 0x60, v4
	v_lshrrev_b32_e32 v240, 6, v1
	v_and_b32_e32 v240, 3, v240
	v_lshl_add_u32 v4, v240, 8, v4
	v_add_u32_e32 v240, v3, v4
	v_mov_b32_e32 v2, v1
	v_mov_b32_e32 v241, 1
	v_ashrrev_i32_e32 v4, 31, v2
	v_lshrrev_b32_e32 v4, 26, v4
	v_lshlrev_b32_e32 v3, 4, v2
	v_add_u32_e32 v4, v2, v4
	v_bfe_i32 v2, v2, 27, 1
	v_lshrrev_b32_e32 v2, 22, v2
	v_add_u32_e32 v2, v3, v2
	v_and_b32_e32 v2, 0xfffffc00, v2
	v_sub_u32_e32 v2, v3, v2
	v_lshrrev_b32_e32 v5, 4, v2
	v_bitop3_b32 v2, v5, v2, 32 bitop3:0x6c
	v_ashrrev_i32_e32 v6, 31, v2
	v_lshrrev_b32_e32 v6, 26, v6
	v_add_u32_e32 v6, v2, v6
	v_ashrrev_i32_e32 v7, 6, v6
	v_and_b32_e32 v6, 0xc0, v6
	v_ashrrev_i32_e32 v4, 6, v4
	v_sub_u32_e32 v2, v2, v6
	v_lshlrev_b32_e32 v5, 3, v4
	v_lshlrev_b32_e32 v4, 5, v4
	v_ashrrev_i16_sdwa v2, v241, sext(v2) dst_sel:DWORD dst_unused:UNUSED_PAD src0_sel:DWORD src1_sel:BYTE_0
	v_and_b32_e32 v4, 32, v4
	v_bfe_i32 v2, v2, 0, 16
	v_add_lshl_u32 v34, v4, v2, 1
	v_add_u32_e32 v2, 0x2000, v3
	v_ashrrev_i32_e32 v3, 31, v2
	v_lshrrev_b32_e32 v3, 22, v3
	v_add_u32_e32 v3, v2, v3
	v_ashrrev_i32_e32 v3, 10, v3
	v_mul_i32_i24_e32 v4, 0x400, v3
	v_sub_u32_e32 v2, v2, v4
	v_lshrrev_b32_e32 v4, 4, v2
	v_bitop3_b32 v2, v4, v2, 32 bitop3:0x6c
	v_ashrrev_i32_e32 v6, 31, v2
	v_lshrrev_b32_e32 v6, 26, v6
	v_and_b32_e32 v5, -16, v5
	v_add_u32_e32 v6, v2, v6
	s_ashr_i32 s1, s5, 8
	v_add_u32_e32 v5, v7, v5
	v_ashrrev_i32_e32 v7, 6, v6
	v_and_b32_e32 v6, 0xc0, v6
	s_lshl_b32 s6, s1, 14
	v_sub_u32_e32 v2, v2, v6
	s_add_i32 s11, s6, 0
	v_lshlrev_b32_e32 v4, 3, v3
	v_lshlrev_b32_e32 v3, 5, v3
	v_ashrrev_i16_sdwa v2, v241, sext(v2) dst_sel:DWORD dst_unused:UNUSED_PAD src0_sel:DWORD src1_sel:BYTE_0
	s_add_u32 s34, s76, 0x10000000
	v_and_b32_e32 v4, -16, v4
	v_and_b32_e32 v3, 32, v3
	v_bfe_i32 v2, v2, 0, 16
	s_addc_u32 s35, s77, 0
	v_add_u32_e32 v4, v7, v4
	v_add_lshl_u32 v35, v3, v2, 1
	v_add_u32_e32 v2, s43, v5
	s_add_i32 s6, s36, -1
	v_min_i32_e32 v37, s6, v2
	v_add_u32_e32 v2, s43, v4
	s_add_i32 s7, s43, 0x80
	v_min_i32_e32 v38, s6, v2
	v_add_u32_e32 v2, s7, v5
	v_min_i32_e32 v39, s6, v2
	v_add_u32_e32 v2, s7, v4
	v_min_i32_e32 v40, s6, v2
	s_add_u32 s6, s34, s2
	s_addc_u32 s7, s35, s3
	s_lshl_b32 s2, s33, 8
	s_ashr_i32 s3, s2, 31
	s_lshl_b64 s[2:3], s[2:3], 2
	s_add_u32 s8, s6, s2
	s_addc_u32 s9, s7, s3
	s_lshl_b32 s2, s1, 3
	s_ashr_i32 s3, s2, 31
	s_lshl_b64 s[6:7], s[2:3], 2
	s_add_u32 s2, s8, s6
	s_addc_u32 s3, s9, s7
	s_add_u32 s8, s2, 0x1000
	global_load_dwordx4 v[2:5], v240, s[2:3] offset:0
	s_addc_u32 s9, s3, 0
	global_load_dwordx4 v[6:9], v240, s[8:9] offset:0
	s_add_u32 s8, s2, 0x2000
	s_addc_u32 s9, s3, 0
	global_load_dwordx4 v[10:13], v240, s[8:9] offset:0
	s_add_u32 s8, s2, 0x3000
	s_addc_u32 s9, s3, 0
	global_load_dwordx4 v[14:17], v240, s[8:9] offset:0
	s_add_u32 s8, s2, 0x4000
	s_addc_u32 s9, s3, 0
	global_load_dwordx4 v[18:21], v240, s[8:9] offset:0
	s_add_u32 s8, s2, 0x5000
	s_addc_u32 s9, s3, 0
	global_load_dwordx4 v[22:25], v240, s[8:9] offset:0
	s_add_u32 s8, s2, 0x6000
	s_addc_u32 s9, s3, 0
	global_load_dwordx4 v[26:29], v240, s[8:9] offset:0
	s_add_u32 s8, s2, 0x7000
	s_addc_u32 s9, s3, 0
	global_load_dwordx4 v[30:33], v240, s[8:9] offset:0
	s_add_i32 s37, s10, 0
	v_readlane_b32 s8, v254, 53
	v_lshl_add_u32 v226, v37, 9, v34
	s_mov_b32 m0, s37
	v_readlane_b32 s9, v254, 54
	s_add_i32 s38, s37, 0x2000
	v_lshl_add_u32 v228, v38, 9, v35
	s_add_i32 s39, s37, 0x4000
	v_lshl_add_u32 v230, v39, 9, v34
	s_add_i32 s40, s37, 0x6000
	global_load_lds_dwordx4 v226, s[8:9]
	s_mov_b32 m0, s38
	v_lshl_add_u32 v232, v40, 9, v35
	global_load_lds_dwordx4 v228, s[8:9]
	s_mov_b32 m0, s39
	v_lshlrev_b32_e32 v34, 2, v1
	global_load_lds_dwordx4 v230, s[8:9]
	s_mov_b32 m0, s40
	v_and_b32_e32 v35, 16, v34
	global_load_lds_dwordx4 v232, s[8:9]
	s_add_u32 s8, s90, 0x27340080
	s_addc_u32 s9, s91, 0
	s_add_i32 s41, s37, 0x8000
	s_mov_b32 m0, s41
	s_add_i32 s42, s37, 0xa000
	global_load_lds_dwordx4 v226, s[8:9]
	s_mov_b32 m0, s42
	v_lshl_or_b32 v35, s0, 5, v35
	global_load_lds_dwordx4 v228, s[8:9]
	v_lshrrev_b32_e32 v35, 3, v35
	v_bfe_u32 v37, v1, 5, 1
	v_or_b32_e32 v35, v35, v37
	v_lshlrev_b32_e32 v37, 8, v1
	v_lshlrev_b32_e32 v38, 1, v1
	v_lshlrev_b32_e32 v39, 10, v35
	v_lshlrev_b32_e32 v35, 4, v1
	v_and_b32_e32 v37, 0x300, v37
	v_and_b32_e32 v38, 48, v38
	v_and_b32_e32 v40, 32, v35
	v_bitop3_b32 v37, v37, v40, v38 bitop3:0x36
	v_add3_u32 v37, s11, v37, v39
	v_lshl_or_b32 v242, v36, 6, v37
	v_lshrrev_b32_e32 v39, 8, v1
	v_lshrrev_b32_e32 v36, 2, v1
	v_and_b32_e32 v36, 1, v36
	v_lshl_or_b32 v36, v39, 1, v36
	v_lshlrev_b32_e32 v37, 8, v36
	v_lshl_or_b32 v37, v36, 6, v37
	v_lshlrev_b32_e32 v38, 1, v1
	v_and_b32_e32 v38, 48, v38
	v_or_b32_e32 v37, v37, v38
	v_lshlrev_b32_e32 v38, 5, v39
	v_xor_b32_e32 v37, v37, v38
	v_lshlrev_b32_e32 v38, 13, v1
	v_and_b32_e32 v38, 0x4000, v38
	v_or_b32_e32 v37, v37, v38
	v_and_b32_e32 v38, 1, v1
	v_bfe_u32 v36, v1, 5, 1
	v_lshl_or_b32 v38, v38, 1, v36
	v_lshrrev_b32_e32 v39, 6, v1
	v_and_b32_e32 v39, 3, v39
	v_lshl_or_b32 v38, v39, 2, v38
	v_lshl_or_b32 v242, v38, 10, v37
	v_mov_b32_e32 v36, v242
	s_waitcnt vmcnt(0)
; #define PG8_BWAIT(n) asm volatile("s_waitcnt vmcnt(" #n ")" : "+v"(bv[0]), "+v"(bv[1]), "+v"(bv[2]), "+v"(bv[3]), "+v"(bv[4]), "+v"(bv[5]), "+v"(bv[6]), "+v"(bv[7]) :: "memory")
; #define PG8_WAIT_V(n) asm volatile("s_waitcnt vmcnt(" #n ")" ::: "memory")
; #define PG8_WAIT_L(n) asm volatile("s_waitcnt lgkmcnt(" #n ")" ::: "memory")
; #define PG8_BAR __builtin_amdgcn_s_barrier()
; #define PG8_SCHED __builtin_amdgcn_sched_barrier(0)
; template <class Epi, class Sched, bool ALIGN_EPI>
; __device__ __forceinline__ void gemm_phase(LAS unsigned char* lds, const Gemm g, const Sched& S, const Epi& E) {
;     ...
;         PG8_BWAIT(0); PG8_BCOMMIT(0); PG8_SCHED; PG8_BISSUE(pbc + (size_t)64 * Sched::LDN);
;         PG8_BWAIT(0); PG8_BCOMMIT(1); PG8_SCHED; PG8_BISSUE(pbc + (size_t)128 * Sched::LDN);
;         PG8_WAIT_V(8); PG8_WAIT_L(0);
;         if (wr == 1) PG8_BAR;
;         PG8_BAR; PG8_BAR;
	s_mov_b32 s9, 0
	v_add_u32_e32 v40, 0x10000, v36
	v_cvt_pk_bf16_f32 v36, v2, v6
	v_cvt_pk_bf16_f32 v37, v10, v14
	v_cvt_pk_bf16_f32 v38, v18, v22
	v_cvt_pk_bf16_f32 v39, v26, v30
	ds_write_b128 v40, v[36:39]
	s_nop 1
	v_cvt_pk_bf16_f32 v36, v3, v7
	v_cvt_pk_bf16_f32 v37, v11, v15
	v_cvt_pk_bf16_f32 v38, v19, v23
	v_cvt_pk_bf16_f32 v39, v27, v31
	v_xor_b32_e32 v2, 64, v40
	ds_write_b128 v2, v[36:39]
	s_nop 1
	v_cvt_pk_bf16_f32 v36, v4, v8
	v_cvt_pk_bf16_f32 v37, v12, v16
	v_cvt_pk_bf16_f32 v38, v20, v24
	v_cvt_pk_bf16_f32 v39, v28, v32
	v_xor_b32_e32 v2, 0x80, v40
	ds_write_b128 v2, v[36:39]
	s_nop 1
	v_cvt_pk_bf16_f32 v2, v5, v9
	v_cvt_pk_bf16_f32 v3, v13, v17
	v_cvt_pk_bf16_f32 v4, v21, v25
	v_cvt_pk_bf16_f32 v5, v29, v33
	v_xor_b32_e32 v6, 0xc0, v40
	ds_write_b128 v6, v[2:5]
	s_nop 1
	s_add_u32 s10, s2, 0x40000
	s_addc_u32 s11, s3, 0
	s_add_u32 s12, s10, 0x1000
	global_load_dwordx4 v[2:5], v240, s[10:11] offset:0
	s_addc_u32 s13, s11, 0
	global_load_dwordx4 v[6:9], v240, s[12:13] offset:0
	s_add_u32 s12, s10, 0x2000
	s_addc_u32 s13, s11, 0
	global_load_dwordx4 v[10:13], v240, s[12:13] offset:0
	s_add_u32 s12, s10, 0x3000
	s_addc_u32 s13, s11, 0
	global_load_dwordx4 v[14:17], v240, s[12:13] offset:0
	s_add_u32 s12, s10, 0x4000
	s_addc_u32 s13, s11, 0
	global_load_dwordx4 v[18:21], v240, s[12:13] offset:0
	s_add_u32 s12, s10, 0x5000
	s_addc_u32 s13, s11, 0
	global_load_dwordx4 v[22:25], v240, s[12:13] offset:0
	s_add_u32 s12, s10, 0x6000
	s_addc_u32 s13, s11, 0
	global_load_dwordx4 v[26:29], v240, s[12:13] offset:0
	s_add_u32 s10, s10, 0x7000
	s_addc_u32 s11, s11, 0
	global_load_dwordx4 v[30:33], v240, s[10:11] offset:0
	v_mov_b32_e32 v36, v242
	s_waitcnt vmcnt(0)
	s_nop 0
	v_add_u32_e32 v40, 0x18000, v36
	v_cvt_pk_bf16_f32 v36, v2, v6
	v_cvt_pk_bf16_f32 v37, v10, v14
	v_cvt_pk_bf16_f32 v38, v18, v22
	v_cvt_pk_bf16_f32 v39, v26, v30
	ds_write_b128 v40, v[36:39]
	s_nop 1
	v_cvt_pk_bf16_f32 v36, v3, v7
	v_cvt_pk_bf16_f32 v37, v11, v15
	v_cvt_pk_bf16_f32 v38, v19, v23
	v_cvt_pk_bf16_f32 v39, v27, v31
	v_xor_b32_e32 v2, 64, v40
	ds_write_b128 v2, v[36:39]
	s_nop 1
	v_cvt_pk_bf16_f32 v36, v4, v8
	v_cvt_pk_bf16_f32 v37, v12, v16
	v_cvt_pk_bf16_f32 v38, v20, v24
	v_cvt_pk_bf16_f32 v39, v28, v32
	v_xor_b32_e32 v2, 0x80, v40
	ds_write_b128 v2, v[36:39]
	s_nop 1
	v_cvt_pk_bf16_f32 v2, v5, v9
	v_cvt_pk_bf16_f32 v3, v13, v17
	v_cvt_pk_bf16_f32 v4, v21, v25
	v_cvt_pk_bf16_f32 v5, v29, v33
	v_xor_b32_e32 v6, 0xc0, v40
	ds_write_b128 v6, v[2:5]
	s_nop 1
	s_add_u32 s10, s2, 0x80000
	s_addc_u32 s11, s3, 0
	s_add_u32 s12, s10, 0x1000
	global_load_dwordx4 v[2:5], v240, s[10:11] offset:0
	s_addc_u32 s13, s11, 0
	global_load_dwordx4 v[6:9], v240, s[12:13] offset:0
	s_add_u32 s12, s10, 0x2000
	s_addc_u32 s13, s11, 0
	global_load_dwordx4 v[10:13], v240, s[12:13] offset:0
	s_add_u32 s12, s10, 0x3000
	s_addc_u32 s13, s11, 0
	global_load_dwordx4 v[14:17], v240, s[12:13] offset:0
	s_add_u32 s12, s10, 0x4000
	s_addc_u32 s13, s11, 0
	global_load_dwordx4 v[18:21], v240, s[12:13] offset:0
	s_add_u32 s12, s10, 0x5000
	s_addc_u32 s13, s11, 0
	global_load_dwordx4 v[22:25], v240, s[12:13] offset:0
	s_add_u32 s12, s10, 0x6000
	s_addc_u32 s13, s11, 0
	global_load_dwordx4 v[26:29], v240, s[12:13] offset:0
	s_add_u32 s10, s10, 0x7000
	s_addc_u32 s11, s11, 0
	global_load_dwordx4 v[30:33], v240, s[10:11] offset:0
	s_waitcnt vmcnt(8)
	s_waitcnt lgkmcnt(0)
	s_cmp_eq_u32 s1, 1
	s_cselect_b64 s[10:11], -1, 0
	s_cmp_lg_u32 s1, 1
	s_cbranch_scc1 .LBB0_4891
	s_barrier
